# grid barrier: cache invalidate issued after the last-arriver decision and release adds (was right behind the returning arrive add)
# baseline (speedup 1.0000x reference)
.LBB0_230:
	v_writelane_b32 v253, s40, 46
	s_cmp_gt_i32 s81, 1
	s_cselect_b64 s[4:5], -1, 0
	v_writelane_b32 v253, s41, 47
	v_writelane_b32 v253, s42, 48
	v_writelane_b32 v253, s43, 49
	v_writelane_b32 v253, s44, 50
	v_writelane_b32 v253, s45, 51
	v_writelane_b32 v253, s46, 52
	v_writelane_b32 v253, s47, 53
	v_writelane_b32 v253, s48, 54
	v_writelane_b32 v253, s49, 55
	v_writelane_b32 v253, s50, 56
	v_writelane_b32 v253, s51, 57
	v_writelane_b32 v253, s52, 58
	v_writelane_b32 v253, s53, 59
	s_and_b64 s[0:1], s[0:1], s[4:5]
	v_writelane_b32 v253, s54, 60
	s_andn2_b64 vcc, exec, s[0:1]
	v_writelane_b32 v253, s55, 61
	s_cbranch_vccnz .LBB0_284
	s_waitcnt vmcnt(0)
	s_barrier
	s_and_saveexec_b64 s[0:1], s[78:79]
	s_cbranch_execz .LBB0_283
	v_mov_b32_e32 v1, 0x22160
	s_waitcnt vmcnt(0) lgkmcnt(0)
	ds_read_b32 v2, v1
	v_mov_b32_e32 v3, 1
	v_mov_b32_e32 v4, s99
	v_and_b32_e32 v5, 0xffff, v4
	v_lshrrev_b32_e32 v6, 16, v4
	global_atomic_add v7, v5, v3, s[100:101] sc0
	v_lshrrev_b32_e32 v8, 8, v5
	v_sub_u32_e32 v8, s98, v8
	v_add_u32_e32 v8, 7, v8
	v_lshrrev_b32_e32 v8, 3, v8
	v_mov_b32_e32 v9, s98
	v_min_u32_e32 v9, 8, v9
	v_mov_b32_e32 v10, 0
	s_waitcnt lgkmcnt(0)
	v_add_u32_e32 v2, 1, v2
	ds_write_b32 v1, v2
	v_mul_lo_u32 v8, v8, v2
	v_mul_lo_u32 v9, v9, v2
	s_waitcnt vmcnt(0)
	v_add_u32_e32 v7, 1, v7
	v_cmp_eq_u32_e32 vcc, v7, v8
	s_cbranch_vccz .Lgb_inv_0
	v_mov_b32_e32 v4, 0
	global_atomic_add v4, v3, s[100:101] offset:2048
	global_atomic_add v4, v3, s[100:101] offset:2304
	global_atomic_add v4, v3, s[100:101] offset:2560
	global_atomic_add v4, v3, s[100:101] offset:2816
	global_atomic_add v4, v3, s[100:101] offset:3072
	global_atomic_add v4, v3, s[100:101] offset:3328
	global_atomic_add v4, v3, s[100:101] offset:3584
	global_atomic_add v4, v3, s[100:101] offset:3840

.LBB0_306:
	s_cmp_gt_i32 s81, 2
	s_cselect_b64 s[4:5], -1, 0
	s_and_b64 s[0:1], s[0:1], s[4:5]
	s_andn2_b64 vcc, exec, s[0:1]
	s_cbranch_vccnz .LBB0_360
	s_waitcnt vmcnt(0)
	s_waitcnt vmcnt(0)
	s_barrier
	s_and_saveexec_b64 s[0:1], s[78:79]
	s_cbranch_execz .LBB0_359
	v_mov_b32_e32 v1, 0x22160
	s_waitcnt vmcnt(0) lgkmcnt(0)
	ds_read_b32 v2, v1
	v_mov_b32_e32 v3, 1
	v_mov_b32_e32 v4, s99
	v_and_b32_e32 v5, 0xffff, v4
	v_lshrrev_b32_e32 v6, 16, v4
	global_atomic_add v7, v5, v3, s[100:101] sc0
	v_lshrrev_b32_e32 v8, 8, v5
	v_sub_u32_e32 v8, s98, v8
	v_add_u32_e32 v8, 7, v8
	v_lshrrev_b32_e32 v8, 3, v8
	v_mov_b32_e32 v9, s98
	v_min_u32_e32 v9, 8, v9
	v_mov_b32_e32 v10, 0
	s_waitcnt lgkmcnt(0)
	v_add_u32_e32 v2, 1, v2
	ds_write_b32 v1, v2
	v_mul_lo_u32 v8, v8, v2
	v_mul_lo_u32 v9, v9, v2
	s_waitcnt vmcnt(0)
	v_add_u32_e32 v7, 1, v7
	v_cmp_eq_u32_e32 vcc, v7, v8
	s_cbranch_vccz .Lgb_inv_1
	v_mov_b32_e32 v4, 0
	global_atomic_add v4, v3, s[100:101] offset:2048
	global_atomic_add v4, v3, s[100:101] offset:2304
	global_atomic_add v4, v3, s[100:101] offset:2560
	global_atomic_add v4, v3, s[100:101] offset:2816
	global_atomic_add v4, v3, s[100:101] offset:3072
	global_atomic_add v4, v3, s[100:101] offset:3328
	global_atomic_add v4, v3, s[100:101] offset:3584
	global_atomic_add v4, v3, s[100:101] offset:3840

.LBB0_427:
	s_cmp_gt_i32 s81, 3
	s_cselect_b64 s[4:5], -1, 0
	s_and_b64 s[6:7], s[36:37], s[4:5]
	s_andn2_b64 vcc, exec, s[6:7]
	s_cbranch_vccnz .LBB0_481
	s_waitcnt vmcnt(0)
	s_waitcnt vmcnt(0)
	s_barrier
	s_and_saveexec_b64 s[6:7], s[78:79]
	s_cbranch_execz .LBB0_480
	v_mov_b32_e32 v1, 0x22160
	s_waitcnt vmcnt(0) lgkmcnt(0)
	ds_read_b32 v2, v1
	v_mov_b32_e32 v3, 1
	v_mov_b32_e32 v4, s99
	v_and_b32_e32 v5, 0xffff, v4
	v_lshrrev_b32_e32 v6, 16, v4
	global_atomic_add v7, v5, v3, s[100:101] sc0
	v_lshrrev_b32_e32 v8, 8, v5
	v_sub_u32_e32 v8, s98, v8
	v_add_u32_e32 v8, 7, v8
	v_lshrrev_b32_e32 v8, 3, v8
	v_mov_b32_e32 v9, s98
	v_min_u32_e32 v9, 8, v9
	v_mov_b32_e32 v10, 0
	s_waitcnt lgkmcnt(0)
	v_add_u32_e32 v2, 1, v2
	ds_write_b32 v1, v2
	v_mul_lo_u32 v8, v8, v2
	v_mul_lo_u32 v9, v9, v2
	s_waitcnt vmcnt(0)
	v_add_u32_e32 v7, 1, v7
	v_cmp_eq_u32_e32 vcc, v7, v8
	s_cbranch_vccz .Lgb_inv_2
	v_mov_b32_e32 v4, 0
	global_atomic_add v4, v3, s[100:101] offset:2048
	global_atomic_add v4, v3, s[100:101] offset:2304
	global_atomic_add v4, v3, s[100:101] offset:2560
	global_atomic_add v4, v3, s[100:101] offset:2816
	global_atomic_add v4, v3, s[100:101] offset:3072
	global_atomic_add v4, v3, s[100:101] offset:3328
	global_atomic_add v4, v3, s[100:101] offset:3584
	global_atomic_add v4, v3, s[100:101] offset:3840

.Lgw_end_2:
	v_mov_b32_e32 v7, 0x22160
	s_waitcnt vmcnt(0) lgkmcnt(0)
	ds_read_b32 v8, v7
	v_mov_b32_e32 v9, 1
	v_mov_b32_e32 v10, s99
	v_and_b32_e32 v11, 0xffff, v10
	v_lshrrev_b32_e32 v12, 16, v10
	global_atomic_add v13, v11, v9, s[100:101] sc0
	v_lshrrev_b32_e32 v14, 8, v11
	v_sub_u32_e32 v14, s98, v14
	v_add_u32_e32 v14, 7, v14
	v_lshrrev_b32_e32 v14, 3, v14
	v_mov_b32_e32 v15, s98
	v_min_u32_e32 v15, 8, v15
	v_mov_b32_e32 v16, 0
	s_waitcnt lgkmcnt(0)
	v_add_u32_e32 v8, 1, v8
	ds_write_b32 v7, v8
	v_mul_lo_u32 v14, v14, v8
	v_mul_lo_u32 v15, v15, v8
	s_waitcnt vmcnt(0)
	v_add_u32_e32 v13, 1, v13
	v_cmp_eq_u32_e32 vcc, v13, v14
	s_cbranch_vccz .Lgb_inv_3
	v_mov_b32_e32 v10, 0
	global_atomic_add v10, v9, s[100:101] offset:2048
	global_atomic_add v10, v9, s[100:101] offset:2304
	global_atomic_add v10, v9, s[100:101] offset:2560
	global_atomic_add v10, v9, s[100:101] offset:2816
	global_atomic_add v10, v9, s[100:101] offset:3072
	global_atomic_add v10, v9, s[100:101] offset:3328
	global_atomic_add v10, v9, s[100:101] offset:3584
	global_atomic_add v10, v9, s[100:101] offset:3840

.LBB0_759:
	s_cmp_gt_i32 s81, 4
	s_cselect_b64 s[0:1], -1, 0
	s_and_b64 s[4:5], s[4:5], s[0:1]
	s_andn2_b64 vcc, exec, s[4:5]
	s_cbranch_vccnz .LBB0_813
	s_waitcnt vmcnt(0)
	s_waitcnt vmcnt(0)
	s_barrier
	s_and_saveexec_b64 s[4:5], s[78:79]
	s_cbranch_execz .LBB0_812
	v_mov_b32_e32 v1, 0x22160
	s_waitcnt vmcnt(0) lgkmcnt(0)
	ds_read_b32 v2, v1
	v_mov_b32_e32 v3, 1
	v_mov_b32_e32 v4, s99
	v_and_b32_e32 v5, 0xffff, v4
	v_lshrrev_b32_e32 v6, 16, v4
	global_atomic_add v7, v5, v3, s[100:101] sc0
	v_lshrrev_b32_e32 v8, 8, v5
	v_sub_u32_e32 v8, s98, v8
	v_add_u32_e32 v8, 7, v8
	v_lshrrev_b32_e32 v8, 3, v8
	v_mov_b32_e32 v9, s98
	v_min_u32_e32 v9, 8, v9
	v_mov_b32_e32 v10, 0
	s_waitcnt lgkmcnt(0)
	v_add_u32_e32 v2, 1, v2
	ds_write_b32 v1, v2
	v_mul_lo_u32 v8, v8, v2
	v_mul_lo_u32 v9, v9, v2
	s_waitcnt vmcnt(0)
	v_add_u32_e32 v7, 1, v7
	v_cmp_eq_u32_e32 vcc, v7, v8
	s_cbranch_vccz .Lgb_inv_4
	v_mov_b32_e32 v4, 0
	global_atomic_add v4, v3, s[100:101] offset:2048
	global_atomic_add v4, v3, s[100:101] offset:2304
	global_atomic_add v4, v3, s[100:101] offset:2560
	global_atomic_add v4, v3, s[100:101] offset:2816
	global_atomic_add v4, v3, s[100:101] offset:3072
	global_atomic_add v4, v3, s[100:101] offset:3328
	global_atomic_add v4, v3, s[100:101] offset:3584
	global_atomic_add v4, v3, s[100:101] offset:3840

.LBB0_843:
	s_cmp_gt_i32 s81, 5
	s_cselect_b64 s[4:5], -1, 0
	s_and_b64 s[0:1], s[0:1], s[4:5]
	s_andn2_b64 vcc, exec, s[0:1]
	s_cbranch_vccnz .LBB0_897
	s_waitcnt vmcnt(0)
	s_waitcnt vmcnt(0)
	s_barrier
	s_and_saveexec_b64 s[0:1], s[78:79]
	s_cbranch_execz .LBB0_896
	v_mov_b32_e32 v1, 0x22160
	s_waitcnt vmcnt(0) lgkmcnt(0)
	ds_read_b32 v2, v1
	v_mov_b32_e32 v3, 1
	v_mov_b32_e32 v4, s99
	v_and_b32_e32 v5, 0xffff, v4
	v_lshrrev_b32_e32 v6, 16, v4
	global_atomic_add v7, v5, v3, s[100:101] sc0
	v_lshrrev_b32_e32 v8, 8, v5
	v_sub_u32_e32 v8, s98, v8
	v_add_u32_e32 v8, 7, v8
	v_lshrrev_b32_e32 v8, 3, v8
	v_mov_b32_e32 v9, s98
	v_min_u32_e32 v9, 8, v9
	v_mov_b32_e32 v10, 0
	s_waitcnt lgkmcnt(0)
	v_add_u32_e32 v2, 1, v2
	ds_write_b32 v1, v2
	v_mul_lo_u32 v8, v8, v2
	v_mul_lo_u32 v9, v9, v2
	s_waitcnt vmcnt(0)
	v_add_u32_e32 v7, 1, v7
	v_cmp_eq_u32_e32 vcc, v7, v8
	s_cbranch_vccz .Lgb_inv_5
	v_mov_b32_e32 v4, 0
	global_atomic_add v4, v3, s[100:101] offset:2048
	global_atomic_add v4, v3, s[100:101] offset:2304
	global_atomic_add v4, v3, s[100:101] offset:2560
	global_atomic_add v4, v3, s[100:101] offset:2816
	global_atomic_add v4, v3, s[100:101] offset:3072
	global_atomic_add v4, v3, s[100:101] offset:3328
	global_atomic_add v4, v3, s[100:101] offset:3584
	global_atomic_add v4, v3, s[100:101] offset:3840

.LBB0_944:
	s_cmp_gt_i32 s81, 6
	s_cselect_b64 s[4:5], -1, 0
	s_and_b64 s[0:1], s[0:1], s[4:5]
	s_andn2_b64 vcc, exec, s[0:1]
	s_cbranch_vccnz .LBB0_998
	s_waitcnt vmcnt(0)
	s_waitcnt vmcnt(0)
	s_barrier
	s_and_saveexec_b64 s[0:1], s[78:79]
	s_cbranch_execz .LBB0_997
	v_mov_b32_e32 v1, 0x22160
	s_waitcnt vmcnt(0) lgkmcnt(0)
	ds_read_b32 v2, v1
	v_mov_b32_e32 v3, 1
	v_mov_b32_e32 v4, s99
	v_and_b32_e32 v5, 0xffff, v4
	v_lshrrev_b32_e32 v6, 16, v4
	global_atomic_add v7, v5, v3, s[100:101] sc0
	v_lshrrev_b32_e32 v8, 8, v5
	v_sub_u32_e32 v8, s98, v8
	v_add_u32_e32 v8, 7, v8
	v_lshrrev_b32_e32 v8, 3, v8
	v_mov_b32_e32 v9, s98
	v_min_u32_e32 v9, 8, v9
	v_mov_b32_e32 v10, 0
	s_waitcnt lgkmcnt(0)
	v_add_u32_e32 v2, 1, v2
	ds_write_b32 v1, v2
	v_mul_lo_u32 v8, v8, v2
	v_mul_lo_u32 v9, v9, v2
	s_waitcnt vmcnt(0)
	v_add_u32_e32 v7, 1, v7
	v_cmp_eq_u32_e32 vcc, v7, v8
	s_cbranch_vccz .Lgb_inv_6
	v_mov_b32_e32 v4, 0
	global_atomic_add v4, v3, s[100:101] offset:2048
	global_atomic_add v4, v3, s[100:101] offset:2304
	global_atomic_add v4, v3, s[100:101] offset:2560
	global_atomic_add v4, v3, s[100:101] offset:2816
	global_atomic_add v4, v3, s[100:101] offset:3072
	global_atomic_add v4, v3, s[100:101] offset:3328
	global_atomic_add v4, v3, s[100:101] offset:3584
	global_atomic_add v4, v3, s[100:101] offset:3840

.Lcv_skip:
	s_cmp_gt_i32 s81, 7
	s_cselect_b64 s[4:5], -1, 0
	s_and_b64 s[0:1], s[76:77], s[4:5]
	v_readlane_b32 s86, v253, 40
	s_andn2_b64 vcc, exec, s[0:1]
	v_readlane_b32 s76, v253, 62
	v_readlane_b32 s77, v253, 63
	v_readlane_b32 s87, v253, 41
	s_cbranch_vccnz .LBB0_1205
	s_waitcnt vmcnt(0)
	s_waitcnt vmcnt(0) lgkmcnt(0)
	s_barrier
	s_and_saveexec_b64 s[0:1], s[78:79]
	s_cbranch_execz .LBB0_1204
	v_mov_b32_e32 v1, 0x22160
	s_waitcnt vmcnt(0) lgkmcnt(0)
	ds_read_b32 v2, v1
	v_mov_b32_e32 v3, 1
	v_mov_b32_e32 v4, s99
	v_and_b32_e32 v5, 0xffff, v4
	v_lshrrev_b32_e32 v6, 16, v4
	global_atomic_add v7, v5, v3, s[100:101] sc0
	v_lshrrev_b32_e32 v8, 8, v5
	v_sub_u32_e32 v8, s98, v8
	v_add_u32_e32 v8, 7, v8
	v_lshrrev_b32_e32 v8, 3, v8
	v_mov_b32_e32 v9, s98
	v_min_u32_e32 v9, 8, v9
	v_mov_b32_e32 v10, 0
	s_waitcnt lgkmcnt(0)
	v_add_u32_e32 v2, 1, v2
	ds_write_b32 v1, v2
	v_mul_lo_u32 v8, v8, v2
	v_mul_lo_u32 v9, v9, v2
	s_waitcnt vmcnt(0)
	v_add_u32_e32 v7, 1, v7
	v_cmp_eq_u32_e32 vcc, v7, v8
	s_cbranch_vccz .Lgb_inv_7
	v_mov_b32_e32 v4, 0
	global_atomic_add v4, v3, s[100:101] offset:2048
	global_atomic_add v4, v3, s[100:101] offset:2304
	global_atomic_add v4, v3, s[100:101] offset:2560
	global_atomic_add v4, v3, s[100:101] offset:2816
	global_atomic_add v4, v3, s[100:101] offset:3072
	global_atomic_add v4, v3, s[100:101] offset:3328
	global_atomic_add v4, v3, s[100:101] offset:3584
	global_atomic_add v4, v3, s[100:101] offset:3840

.LBB0_1220:
	s_cmp_gt_i32 s81, 8
	s_cselect_b64 s[14:15], -1, 0
	s_and_b64 s[4:5], s[12:13], s[14:15]
	s_andn2_b64 vcc, exec, s[4:5]
	s_cbranch_vccnz .LBB0_1274
	s_waitcnt vmcnt(0)
	s_waitcnt vmcnt(0) lgkmcnt(0)
	s_barrier
	s_and_saveexec_b64 s[4:5], s[78:79]
	s_cbranch_execz .LBB0_1273
	v_mov_b32_e32 v1, 0x22160
	s_waitcnt vmcnt(0) lgkmcnt(0)
	ds_read_b32 v2, v1
	v_mov_b32_e32 v3, 1
	v_mov_b32_e32 v4, s99
	v_and_b32_e32 v5, 0xffff, v4
	v_lshrrev_b32_e32 v6, 16, v4
	global_atomic_add v7, v5, v3, s[100:101] sc0
	v_lshrrev_b32_e32 v8, 8, v5
	v_sub_u32_e32 v8, s98, v8
	v_add_u32_e32 v8, 7, v8
	v_lshrrev_b32_e32 v8, 3, v8
	v_mov_b32_e32 v9, s98
	v_min_u32_e32 v9, 8, v9
	v_mov_b32_e32 v10, 0
	s_waitcnt lgkmcnt(0)
	v_add_u32_e32 v2, 1, v2
	ds_write_b32 v1, v2
	v_mul_lo_u32 v8, v8, v2
	v_mul_lo_u32 v9, v9, v2
	s_waitcnt vmcnt(0)
	v_add_u32_e32 v7, 1, v7
	v_cmp_eq_u32_e32 vcc, v7, v8
	s_cbranch_vccz .Lgb_inv_8
	v_mov_b32_e32 v4, 0
	global_atomic_add v4, v3, s[100:101] offset:2048
	global_atomic_add v4, v3, s[100:101] offset:2304
	global_atomic_add v4, v3, s[100:101] offset:2560
	global_atomic_add v4, v3, s[100:101] offset:2816
	global_atomic_add v4, v3, s[100:101] offset:3072
	global_atomic_add v4, v3, s[100:101] offset:3328
	global_atomic_add v4, v3, s[100:101] offset:3584
	global_atomic_add v4, v3, s[100:101] offset:3840

.LBB0_1606:
	s_cmp_gt_i32 s81, 10
	s_cselect_b64 s[0:1], -1, 0
	s_and_b64 s[4:5], s[12:13], s[0:1]
	s_andn2_b64 vcc, exec, s[4:5]
	s_waitcnt vmcnt(0)
	v_and_b32_e32 v82, 63, v0
	s_cbranch_vccnz .LBB0_1660
	s_waitcnt vmcnt(0)
	s_waitcnt lgkmcnt(0)
	s_barrier
	s_and_saveexec_b64 s[4:5], s[78:79]
	s_cbranch_execz .LBB0_1659
	v_mov_b32_e32 v1, 0x22160
	s_waitcnt vmcnt(0) lgkmcnt(0)
	ds_read_b32 v2, v1
	v_mov_b32_e32 v3, 1
	v_mov_b32_e32 v4, s99
	v_and_b32_e32 v5, 0xffff, v4
	v_lshrrev_b32_e32 v6, 16, v4
	global_atomic_add v7, v5, v3, s[100:101] sc0
	v_mov_b32_e32 v12, 0
	global_load_dword v11, v12, s[100:101] offset:128 sc1
	v_lshrrev_b32_e32 v8, 8, v5
	v_sub_u32_e32 v8, s98, v8
	v_add_u32_e32 v8, 7, v8
	v_lshrrev_b32_e32 v8, 3, v8
	v_mov_b32_e32 v9, s98
	v_min_u32_e32 v9, 8, v9
	v_mov_b32_e32 v10, 0
	s_waitcnt lgkmcnt(0)
	v_add_u32_e32 v2, 1, v2
	ds_write_b32 v1, v2
	v_mul_lo_u32 v8, v8, v2
	v_mul_lo_u32 v9, v9, v2
	s_waitcnt vmcnt(0)
	v_add_u32_e32 v7, 1, v7
	v_cmp_eq_u32_e32 vcc, v7, v8
	s_cbranch_vccz .Lgb_inv_9
	v_mov_b32_e32 v4, 0
	global_atomic_add v4, v3, s[100:101] offset:2048
	global_atomic_add v4, v3, s[100:101] offset:2304
	global_atomic_add v4, v3, s[100:101] offset:2560
	global_atomic_add v4, v3, s[100:101] offset:2816
	global_atomic_add v4, v3, s[100:101] offset:3072
	global_atomic_add v4, v3, s[100:101] offset:3328
	global_atomic_add v4, v3, s[100:101] offset:3584
	global_atomic_add v4, v3, s[100:101] offset:3840

.LBB0_1750:
	s_waitcnt vmcnt(0)
	s_waitcnt lgkmcnt(0)
	s_barrier
	s_mov_b64 s[6:7], exec
	v_readlane_b32 s40, v253, 46
	s_and_b64 s[8:9], s[6:7], s[78:79]
	v_readlane_b32 s41, v253, 47
	v_readlane_b32 s42, v253, 48
	v_readlane_b32 s43, v253, 49
	v_readlane_b32 s44, v253, 50
	v_readlane_b32 s45, v253, 51
	v_readlane_b32 s52, v253, 58
	v_readlane_b32 s53, v253, 59
	v_readlane_b32 s54, v253, 60
	v_readlane_b32 s55, v253, 61
	v_and_b32_e32 v82, 63, v0
	v_readlane_b32 s46, v253, 52
	v_readlane_b32 s47, v253, 53
	v_readlane_b32 s48, v253, 54
	v_readlane_b32 s49, v253, 55
	v_readlane_b32 s50, v253, 56
	v_readlane_b32 s51, v253, 57
	s_mov_b64 exec, s[8:9]
	s_cbranch_execz .LBB0_1802
	v_mov_b32_e32 v2, 0x22160
	s_waitcnt vmcnt(0) lgkmcnt(0)
	ds_read_b32 v3, v2
	v_mov_b32_e32 v4, 1
	v_mov_b32_e32 v5, s99
	v_and_b32_e32 v6, 0xffff, v5
	v_lshrrev_b32_e32 v7, 16, v5
	global_atomic_add v8, v6, v4, s[100:101] sc0
	v_lshrrev_b32_e32 v9, 8, v6
	v_sub_u32_e32 v9, s98, v9
	v_add_u32_e32 v9, 7, v9
	v_lshrrev_b32_e32 v9, 3, v9
	v_mov_b32_e32 v10, s98
	v_min_u32_e32 v10, 8, v10
	v_mov_b32_e32 v11, 0
	s_waitcnt lgkmcnt(0)
	v_add_u32_e32 v3, 1, v3
	ds_write_b32 v2, v3
	v_mul_lo_u32 v9, v9, v3
	v_mul_lo_u32 v10, v10, v3
	s_waitcnt vmcnt(0)
	v_add_u32_e32 v8, 1, v8
	v_cmp_eq_u32_e32 vcc, v8, v9
	s_cbranch_vccz .Lgb_inv_10
	v_mov_b32_e32 v5, 0
	global_atomic_add v5, v4, s[100:101] offset:2048
	global_atomic_add v5, v4, s[100:101] offset:2304
	global_atomic_add v5, v4, s[100:101] offset:2560
	global_atomic_add v5, v4, s[100:101] offset:2816
	global_atomic_add v5, v4, s[100:101] offset:3072
	global_atomic_add v5, v4, s[100:101] offset:3328
	global_atomic_add v5, v4, s[100:101] offset:3584
	global_atomic_add v5, v4, s[100:101] offset:3840

.LBB0_1811:
	s_cmp_gt_i32 s81, 11
	s_cselect_b64 s[4:5], -1, 0
	s_and_b64 s[0:1], s[0:1], s[4:5]
	v_readlane_b32 s36, v253, 46
	s_andn2_b64 vcc, exec, s[0:1]
	v_readlane_b32 s37, v253, 47
	v_readlane_b32 s38, v253, 48
	v_readlane_b32 s39, v253, 49
	v_readlane_b32 s40, v253, 50
	v_readlane_b32 s41, v253, 51
	v_readlane_b32 s48, v253, 58
	v_readlane_b32 s49, v253, 59
	v_readlane_b32 s50, v253, 60
	v_readlane_b32 s51, v253, 61
	v_readlane_b32 s42, v253, 52
	v_readlane_b32 s43, v253, 53
	v_readlane_b32 s44, v253, 54
	v_readlane_b32 s45, v253, 55
	v_readlane_b32 s46, v253, 56
	v_readlane_b32 s47, v253, 57
	s_cbranch_vccnz .LBB0_1865
	s_waitcnt vmcnt(0)
	s_waitcnt lgkmcnt(0)
	s_barrier
	s_and_saveexec_b64 s[0:1], s[78:79]
	s_cbranch_execz .LBB0_1864
	v_mov_b32_e32 v1, 0x22160
	s_waitcnt vmcnt(0) lgkmcnt(0)
	ds_read_b32 v2, v1
	v_mov_b32_e32 v3, 1
	v_mov_b32_e32 v4, s99
	v_and_b32_e32 v5, 0xffff, v4
	v_lshrrev_b32_e32 v6, 16, v4
	global_atomic_add v7, v5, v3, s[100:101] sc0
	v_lshrrev_b32_e32 v8, 8, v5
	v_sub_u32_e32 v8, s98, v8
	v_add_u32_e32 v8, 7, v8
	v_lshrrev_b32_e32 v8, 3, v8
	v_mov_b32_e32 v9, s98
	v_min_u32_e32 v9, 8, v9
	v_mov_b32_e32 v10, 0
	s_waitcnt lgkmcnt(0)
	v_add_u32_e32 v2, 1, v2
	ds_write_b32 v1, v2
	v_mul_lo_u32 v8, v8, v2
	v_mul_lo_u32 v9, v9, v2
	s_waitcnt vmcnt(0)
	v_add_u32_e32 v7, 1, v7
	v_cmp_eq_u32_e32 vcc, v7, v8
	s_cbranch_vccz .Lgb_inv_11
	v_mov_b32_e32 v4, 0
	global_atomic_add v4, v3, s[100:101] offset:2048
	global_atomic_add v4, v3, s[100:101] offset:2304
	global_atomic_add v4, v3, s[100:101] offset:2560
	global_atomic_add v4, v3, s[100:101] offset:2816
	global_atomic_add v4, v3, s[100:101] offset:3072
	global_atomic_add v4, v3, s[100:101] offset:3328
	global_atomic_add v4, v3, s[100:101] offset:3584
	global_atomic_add v4, v3, s[100:101] offset:3840

.LBB0_1890:
	s_cmp_gt_i32 s81, 12
	s_cselect_b64 s[2:3], -1, 0
	s_and_b64 s[0:1], s[0:1], s[2:3]
	s_andn2_b64 vcc, exec, s[0:1]
	s_cbranch_vccnz .LBB0_1944
	s_waitcnt vmcnt(0)
	s_waitcnt lgkmcnt(0)
	s_barrier
	s_and_saveexec_b64 s[0:1], s[78:79]
	s_cbranch_execz .LBB0_1943
	v_mov_b32_e32 v1, 0x22160
	s_waitcnt vmcnt(0) lgkmcnt(0)
	ds_read_b32 v2, v1
	v_mov_b32_e32 v3, 1
	v_mov_b32_e32 v4, s99
	v_and_b32_e32 v5, 0xffff, v4
	v_lshrrev_b32_e32 v6, 16, v4
	global_atomic_add v7, v5, v3, s[100:101] sc0
	v_lshrrev_b32_e32 v8, 8, v5
	v_sub_u32_e32 v8, s98, v8
	v_add_u32_e32 v8, 7, v8
	v_lshrrev_b32_e32 v8, 3, v8
	v_mov_b32_e32 v9, s98
	v_min_u32_e32 v9, 8, v9
	v_mov_b32_e32 v10, 0
	s_waitcnt lgkmcnt(0)
	v_add_u32_e32 v2, 1, v2
	ds_write_b32 v1, v2
	v_mul_lo_u32 v8, v8, v2
	v_mul_lo_u32 v9, v9, v2
	s_waitcnt vmcnt(0)
	v_add_u32_e32 v7, 1, v7
	v_cmp_eq_u32_e32 vcc, v7, v8
	s_cbranch_vccz .Lgb_inv_12
	v_mov_b32_e32 v4, 0
	global_atomic_add v4, v3, s[100:101] offset:2048
	global_atomic_add v4, v3, s[100:101] offset:2304
	global_atomic_add v4, v3, s[100:101] offset:2560
	global_atomic_add v4, v3, s[100:101] offset:2816
	global_atomic_add v4, v3, s[100:101] offset:3072
	global_atomic_add v4, v3, s[100:101] offset:3328
	global_atomic_add v4, v3, s[100:101] offset:3584
	global_atomic_add v4, v3, s[100:101] offset:3840

.LBB0_1991:
	s_cmp_gt_i32 s81, 13
	s_cselect_b64 s[2:3], -1, 0
	s_and_b64 s[0:1], s[0:1], s[2:3]
	s_andn2_b64 vcc, exec, s[0:1]
	s_cbranch_vccnz .LBB0_2045
	s_waitcnt vmcnt(0)
	s_waitcnt lgkmcnt(0)
	s_barrier
	s_and_saveexec_b64 s[0:1], s[78:79]
	s_cbranch_execz .LBB0_2044
	v_mov_b32_e32 v1, 0x22160
	s_waitcnt vmcnt(0) lgkmcnt(0)
	ds_read_b32 v2, v1
	v_mov_b32_e32 v3, 1
	v_mov_b32_e32 v4, s99
	v_and_b32_e32 v5, 0xffff, v4
	v_lshrrev_b32_e32 v6, 16, v4
	global_atomic_add v7, v5, v3, s[100:101] sc0
	v_lshrrev_b32_e32 v8, 8, v5
	v_sub_u32_e32 v8, s98, v8
	v_add_u32_e32 v8, 7, v8
	v_lshrrev_b32_e32 v8, 3, v8
	v_mov_b32_e32 v9, s98
	v_min_u32_e32 v9, 8, v9
	v_mov_b32_e32 v10, 0
	s_waitcnt lgkmcnt(0)
	v_add_u32_e32 v2, 1, v2
	ds_write_b32 v1, v2
	v_mul_lo_u32 v8, v8, v2
	v_mul_lo_u32 v9, v9, v2
	s_waitcnt vmcnt(0)
	v_add_u32_e32 v7, 1, v7
	v_cmp_eq_u32_e32 vcc, v7, v8
	s_cbranch_vccz .Lgb_inv_13
	v_mov_b32_e32 v4, 0
	global_atomic_add v4, v3, s[100:101] offset:2048
	global_atomic_add v4, v3, s[100:101] offset:2304
	global_atomic_add v4, v3, s[100:101] offset:2560
	global_atomic_add v4, v3, s[100:101] offset:2816
	global_atomic_add v4, v3, s[100:101] offset:3072
	global_atomic_add v4, v3, s[100:101] offset:3328
	global_atomic_add v4, v3, s[100:101] offset:3584
	global_atomic_add v4, v3, s[100:101] offset:3840
